# GLA matrix section: output-row offset math moved off the post-barrier head into the first MFMA group; state-decay scale reads issued 3+1 instead of four dependent LDS round trips
# baseline (speedup 1.0000x reference)
.LBB0_486:
	s_waitcnt lgkmcnt(0)
	s_barrier
	ds_read_b128 v[30:33], v97 offset:9216
	ds_read_b128 v[40:43], v97 offset:9280
	ds_read_b128 v[44:47], v97 offset:11520
	ds_read_b128 v[52:55], v97 offset:2304
	ds_read_b128 v[60:63], v97 offset:11584
	ds_read_b128 v[64:67], v97 offset:2368
	ds_read_b128 v[72:75], v98 offset:9216
	ds_read_b128 v[142:145], v98
	ds_read_b128 v[146:149], v98 offset:9280
	ds_read_b128 v[150:153], v98 offset:64
	ds_read_b128 v[154:157], v99 offset:9216
	ds_read_b128 v[158:161], v99
	ds_read_b128 v[162:165], v99 offset:9280
	ds_read_b128 v[166:169], v99 offset:64
	ds_read_b128 v[48:51], v97 offset:64
	ds_read_b128 v[56:59], v97
	s_waitcnt lgkmcnt(0)
	v_mfma_f32_16x16x32_bf16 v[56:59], v[30:33], v[56:59], 0
	v_mfma_f32_16x16x32_bf16 v[48:51], v[40:43], v[48:51], v[56:59]
	s_nop 7
	v_cndmask_b32_e64 v35, v51, 0, s[40:41]
	v_cndmask_b32_e64 v141, v50, 0, s[62:63]
	v_cndmask_b32_e64 v170, v49, 0, s[72:73]
	v_cndmask_b32_e64 v171, v48, 0, s[2:3]
	v_mfma_f32_16x16x32_bf16 v[48:51], v[30:33], v[52:55], 0
	v_mfma_f32_16x16x32_bf16 v[56:59], v[40:43], v[64:67], v[48:51]
	v_mfma_f32_16x16x32_bf16 v[48:51], v[30:33], v[142:145], 0
	v_mfma_f32_16x16x32_bf16 v[30:33], v[30:33], v[158:161], 0
	v_mfma_f32_16x16x32_bf16 v[48:51], v[40:43], v[150:153], v[48:51]
	v_mfma_f32_16x16x32_bf16 v[40:43], v[40:43], v[166:169], v[30:33]
	v_mfma_f32_16x16x32_bf16 v[30:33], v[44:47], v[52:55], 0
	v_mfma_f32_16x16x32_bf16 v[30:33], v[60:63], v[64:67], v[30:33]
	v_cvt_pk_bf16_f32 v64, v26, v27
	v_cvt_pk_bf16_f32 v65, v28, v29
	v_cvt_pk_bf16_f32 v66, v36, v37
	v_cvt_pk_bf16_f32 v67, v38, v39
	v_and_b32_e32 v176, 15, v127
	v_add_u32_e32 v177, s91, v176
	v_sub_u32_e32 v176, s89, v176
	s_mov_b32 s0, 0x2000
	s_movk_i32 s1, 0x4000
	s_cmp_gt_u32 s92, 3
	s_cbranch_scc0 .Lgo_ctx
	v_add_u32_e32 v215, 0xffffff00, v177
	v_add_u32_e32 v216, 0x8ff, v176
	v_cndmask_b32_e64 v215, v216, v215, s[58:59]
	v_lshlrev_b32_e32 v216, 6, v215
	v_and_b32_e32 v216, 0x7c0, v216
	v_ashrrev_i32_e32 v251, 5, v215
	v_add_u32_e32 v216, v216, v251
	v_cndmask_b32_e64 v215, v216, v215, s[38:39]
	v_add_u32_e32 v215, s90, v215
	s_bitcmp1_b32 s38, 0
	s_cbranch_scc1 .Lgo_row
	s_mov_b32 s0, 0x80000
	s_movk_i32 s1, 0x200
	s_branch .Lgo_row

.Lgo_pos:
	v_lshl_add_u32 v251, v215, 9, v218
	v_add_u32_e32 v252, s0, v251
	v_add_u32_e32 v253, s1, v251
	v_add_u32_e32 v216, s1, v252
	s_nop 3
	v_cndmask_b32_e64 v172, v33, 0, s[40:41]
	v_cndmask_b32_e64 v173, v32, 0, s[62:63]
	v_cndmask_b32_e64 v174, v31, 0, s[72:73]
	v_cndmask_b32_e64 v175, v30, 0, s[2:3]
	v_mfma_f32_16x16x32_bf16 v[30:33], v[44:47], v[142:145], 0
	v_mfma_f32_16x16x32_bf16 v[68:71], v[60:63], v[150:153], v[30:33]
	v_mfma_f32_16x16x32_bf16 v[30:33], v[44:47], v[158:161], 0
	v_mfma_f32_16x16x32_bf16 v[52:55], v[60:63], v[166:169], v[30:33]
	v_cvt_pk_bf16_f32 v60, v18, v19
	v_cvt_pk_bf16_f32 v61, v20, v21
	v_cvt_pk_bf16_f32 v62, v22, v23
	v_mfma_f32_16x16x32_bf16 v[30:33], v[72:75], v[142:145], 0
	v_cvt_pk_bf16_f32 v63, v24, v25
	v_mfma_f32_16x16x32_bf16 v[30:33], v[146:149], v[150:153], v[30:33]
	s_nop 7
	v_cndmask_b32_e64 v150, v33, 0, s[40:41]
	v_cndmask_b32_e64 v151, v32, 0, s[62:63]
	v_cndmask_b32_e64 v152, v31, 0, s[72:73]
	v_cndmask_b32_e64 v153, v30, 0, s[2:3]
	v_mfma_f32_16x16x32_bf16 v[30:33], v[72:75], v[158:161], 0
	v_mfma_f32_16x16x32_bf16 v[44:47], v[146:149], v[166:169], v[30:33]
	v_mfma_f32_16x16x32_bf16 v[30:33], v[154:157], v[158:161], 0
	v_mfma_f32_16x16x32_bf16 v[30:33], v[162:165], v[166:169], v[30:33]
	s_nop 7
	v_cndmask_b32_e64 v157, v30, 0, s[2:3]
	v_add_u32_e32 v30, 0x6800, v106
	ds_read2_b64 v[142:145], v30 offset0:128 offset1:132
	ds_read2_b64 v[72:75], v30 offset0:136 offset1:140
	v_cndmask_b32_e64 v154, v33, 0, s[40:41]
	v_cndmask_b32_e64 v155, v32, 0, s[62:63]
	v_cvt_pk_bf16_f32 v32, v171, v170
	v_cvt_pk_bf16_f32 v33, v141, v35
	v_mov_b32_e32 v35, v34
	ds_read2_b64 v[146:149], v101 offset1:4
	v_cndmask_b32_e64 v156, v31, 0, s[72:73]
	s_waitcnt lgkmcnt(2)
	v_mfma_f32_16x16x32_bf16 v[30:33], v[142:145], v[32:35], 0
	s_waitcnt lgkmcnt(0)
	v_mfma_f32_16x16x32_bf16 v[30:33], v[60:63], v[146:149], v[30:33]
	ds_read2_b64 v[146:149], v101 offset0:8 offset1:12
	s_waitcnt lgkmcnt(0)
	v_mfma_f32_16x16x32_bf16 v[30:33], v[64:67], v[146:149], v[30:33]
	s_nop 7
	v_mul_f32_e32 v30, 4.0, v30
	v_mul_f32_e32 v31, 4.0, v31
	v_mul_f32_e32 v32, 4.0, v32
	v_mul_f32_e32 v33, 4.0, v33
	v_med3_f32 v30, v30, s75, v238
	v_med3_f32 v31, v31, s75, v238
	v_med3_f32 v32, v32, s75, v238
	v_med3_f32 v33, v33, s75, v238
	v_cvt_pk_fp8_f32 v247, v30, v31
	s_nop 1
	v_cvt_pk_fp8_f32 v247, v32, v33 op_sel:[0,0,1]
	s_nop 1
	global_store_dword v251, v247, s[94:95]
	v_cvt_pk_bf16_f32 v30, v56, v57
	v_cvt_pk_bf16_f32 v31, v58, v59
	v_cvt_pk_bf16_f32 v32, v175, v174
	v_cvt_pk_bf16_f32 v33, v173, v172
	ds_read2_b64 v[56:59], v102 offset1:4
	s_nop 0
	v_mfma_f32_16x16x32_bf16 v[30:33], v[142:145], v[30:33], 0
	s_waitcnt lgkmcnt(0)
	v_mfma_f32_16x16x32_bf16 v[30:33], v[60:63], v[56:59], v[30:33]
	ds_read2_b64 v[56:59], v102 offset0:8 offset1:12
	s_waitcnt lgkmcnt(0)
	v_mfma_f32_16x16x32_bf16 v[30:33], v[64:67], v[56:59], v[30:33]
	s_nop 7
	v_mul_f32_e32 v30, 4.0, v30
	v_mul_f32_e32 v31, 4.0, v31
	v_mul_f32_e32 v32, 4.0, v32
	v_mul_f32_e32 v33, 4.0, v33
	v_med3_f32 v30, v30, s75, v238
	v_med3_f32 v31, v31, s75, v238
	v_med3_f32 v32, v32, s75, v238
	v_med3_f32 v33, v33, s75, v238
	v_cvt_pk_fp8_f32 v248, v30, v31
	s_nop 1
	v_cvt_pk_fp8_f32 v248, v32, v33 op_sel:[0,0,1]
	s_nop 1
	global_store_dword v252, v248, s[94:95]
	v_cvt_pk_bf16_f32 v30, v48, v49
	v_cvt_pk_bf16_f32 v31, v50, v51
	v_cvt_pk_bf16_f32 v32, v68, v69
	v_cvt_pk_bf16_f32 v33, v70, v71
	s_nop 1
	v_mfma_f32_16x16x32_bf16 v[48:51], v[142:145], v[30:33], 0
	v_cvt_pk_bf16_f32 v32, v153, v152
	v_cvt_pk_bf16_f32 v33, v151, v150
	s_nop 1
	v_mfma_f32_16x16x32_bf16 v[30:33], v[72:75], v[32:35], v[48:51]
	v_add_u32_e32 v35, v95, v105
	s_nop 1
	ds_read2_b64 v[48:51], v103 offset1:4
	s_waitcnt lgkmcnt(0)
	v_mfma_f32_16x16x32_bf16 v[30:33], v[60:63], v[48:51], v[30:33]
	ds_read2_b64 v[48:51], v103 offset0:8 offset1:12
	s_waitcnt lgkmcnt(0)
	v_mfma_f32_16x16x32_bf16 v[30:33], v[64:67], v[48:51], v[30:33]
	s_nop 7
	v_mul_f32_e32 v30, 4.0, v30
	v_mul_f32_e32 v31, 4.0, v31
	v_mul_f32_e32 v32, 4.0, v32
	v_mul_f32_e32 v33, 4.0, v33
	v_med3_f32 v30, v30, s75, v238
	v_med3_f32 v31, v31, s75, v238
	v_med3_f32 v32, v32, s75, v238
	v_med3_f32 v33, v33, s75, v238
	v_cvt_pk_fp8_f32 v249, v30, v31
	s_nop 1
	v_cvt_pk_fp8_f32 v249, v32, v33 op_sel:[0,0,1]
	s_nop 1
	global_store_dword v253, v249, s[94:95]
	v_cvt_pk_bf16_f32 v30, v40, v41
	v_cvt_pk_bf16_f32 v31, v42, v43
	v_cvt_pk_bf16_f32 v32, v52, v53
	v_cvt_pk_bf16_f32 v33, v54, v55
	v_cvt_pk_bf16_f32 v40, v44, v45
	v_cvt_pk_bf16_f32 v41, v46, v47
	v_mfma_f32_16x16x32_bf16 v[30:33], v[142:145], v[30:33], 0
	v_cvt_pk_bf16_f32 v42, v157, v156
	v_cvt_pk_bf16_f32 v43, v155, v154
	v_add_u32_e32 v44, v95, v100
	s_nop 0
	v_mfma_f32_16x16x32_bf16 v[30:33], v[72:75], v[40:43], v[30:33]
	ds_read2_b64 v[40:43], v104 offset1:4
	s_waitcnt lgkmcnt(0)
	v_mfma_f32_16x16x32_bf16 v[30:33], v[60:63], v[40:43], v[30:33]
	ds_read2_b64 v[40:43], v104 offset0:8 offset1:12
	s_waitcnt lgkmcnt(0)
	v_mfma_f32_16x16x32_bf16 v[30:33], v[64:67], v[40:43], v[30:33]
	s_nop 7
	v_mul_f32_e32 v30, 4.0, v30
	v_mul_f32_e32 v31, 4.0, v31
	v_mul_f32_e32 v32, 4.0, v32
	v_mul_f32_e32 v33, 4.0, v33
	v_med3_f32 v30, v30, s75, v238
	v_med3_f32 v31, v31, s75, v238
	v_med3_f32 v32, v32, s75, v238
	v_med3_f32 v33, v33, s75, v238
	v_cvt_pk_fp8_f32 v250, v30, v31
	s_nop 1
	v_cvt_pk_fp8_f32 v250, v32, v33 op_sel:[0,0,1]
	s_nop 1
	global_store_dword v216, v250, s[94:95]
	ds_read_b128 v[248:251], v114 offset:48128
	ds_read_b64 v[252:253], v114 offset:48192
	ds_read_b64 v[176:177], v114 offset:48200
	ds_read_b128 v[30:33], v114 offset:48320
	ds_read_b128 v[40:43], v44 offset:18432
	s_waitcnt lgkmcnt(0)
	v_pk_mul_f32 v[18:19], v[18:19], v[248:249]
	v_pk_mul_f32 v[20:21], v[20:21], v[250:251]
	ds_read_b128 v[248:251], v114 offset:48256
	v_pk_mul_f32 v[22:23], v[22:23], v[252:253]
	v_pk_mul_f32 v[24:25], v[24:25], v[176:177]
	v_pk_mul_f32 v[30:31], v[36:37], v[30:31]
	v_pk_mul_f32 v[32:33], v[38:39], v[32:33]
	s_waitcnt lgkmcnt(0)
	v_pk_mul_f32 v[26:27], v[26:27], v[248:249]
	v_pk_mul_f32 v[28:29], v[28:29], v[250:251]
	ds_read_b128 v[36:39], v35 offset:27648
	s_waitcnt vmcnt(38)
	v_mov_b32_e32 v115, v178
	v_mov_b32_e32 v116, v179
	v_mov_b32_e32 v117, v180
	v_mov_b32_e32 v118, v181
	v_mov_b32_e32 v119, v182
	v_mov_b32_e32 v120, v183
	s_waitcnt lgkmcnt(0)
	v_mfma_f32_16x16x32_bf16 v[18:21], v[40:43], v[36:39], v[18:21]
	ds_read_b128 v[40:43], v44 offset:20736
	s_waitcnt vmcnt(32)
	v_mov_b32_e32 v121, v184
	v_mov_b32_e32 v122, v185
	v_mov_b32_e32 v123, v186
	v_mov_b32_e32 v124, v187
	v_mov_b32_e32 v125, v188
	v_mov_b32_e32 v128, v189
	s_waitcnt lgkmcnt(0)
	v_mfma_f32_16x16x32_bf16 v[22:25], v[40:43], v[36:39], v[22:25]
	ds_read_b128 v[40:43], v44 offset:23040
	s_waitcnt vmcnt(26)
	v_mov_b32_e32 v129, v190
	v_mov_b32_e32 v130, v192
	v_mov_b32_e32 v131, v194
	v_mov_b32_e32 v132, v196
	v_mov_b32_e32 v133, v200
	v_mov_b32_e32 v134, v201
	s_waitcnt lgkmcnt(0)
	v_mfma_f32_16x16x32_bf16 v[26:29], v[40:43], v[36:39], v[26:29]
	ds_read_b128 v[40:43], v44 offset:25344
	s_waitcnt vmcnt(20)
	v_mov_b32_e32 v135, v202
	v_mov_b32_e32 v136, v203
	v_mov_b32_e32 v137, v206
	v_mov_b32_e32 v138, v207
	v_mov_b32_e32 v139, v208
	v_mov_b32_e32 v140, v209
	s_waitcnt lgkmcnt(0)
	v_mfma_f32_16x16x32_bf16 v[30:33], v[40:43], v[36:39], v[30:33]
	ds_read_b128 v[36:39], v35 offset:27712
	ds_read_b128 v[40:43], v44 offset:18496
	s_waitcnt vmcnt(16)
	v_mov_b32_e32 v2, v220
	v_mov_b32_e32 v1, v219
	v_mov_b32_e32 v4, v222
	v_mov_b32_e32 v3, v221
	s_waitcnt lgkmcnt(0)
	v_mfma_f32_16x16x32_bf16 v[18:21], v[40:43], v[36:39], v[18:21]
	ds_read_b128 v[40:43], v44 offset:20800
	s_waitcnt vmcnt(12)
	v_mov_b32_e32 v6, v224
	v_mov_b32_e32 v5, v223
	v_mov_b32_e32 v8, v226
	v_mov_b32_e32 v7, v225
	s_waitcnt lgkmcnt(0)
	v_mfma_f32_16x16x32_bf16 v[22:25], v[40:43], v[36:39], v[22:25]
	ds_read_b128 v[40:43], v44 offset:23104
	s_waitcnt vmcnt(8)
	v_mov_b32_e32 v10, v228
	v_mov_b32_e32 v9, v227
	v_mov_b32_e32 v12, v230
	v_mov_b32_e32 v11, v229
	s_waitcnt lgkmcnt(0)
	v_mfma_f32_16x16x32_bf16 v[26:29], v[40:43], v[36:39], v[26:29]
	ds_read_b128 v[40:43], v44 offset:25408
	s_waitcnt vmcnt(4)
	v_mov_b32_e32 v14, v232
	v_mov_b32_e32 v13, v231
	v_mov_b32_e32 v16, v246
	v_mov_b32_e32 v15, v233
	s_waitcnt lgkmcnt(0)
	v_mfma_f32_16x16x32_bf16 v[36:39], v[40:43], v[36:39], v[30:33]
	s_nop 2
	s_branch .LBB0_468
